# biasenc
# speedup vs baseline: 1.1567x; 1.0141x over previous
_Z11prep_kernelPKfS0_S0_S0_S0_S0_S0_S0_PhPf:
	s_load_dwordx2 s[6:7], s[0:1], 0x40
	s_load_dwordx2 s[8:9], s[0:1], 0x8
	s_cmp_gt_u32 s2, 21
	s_mov_b64 s[4:5], -1
	s_cbranch_scc0 .LBB0_43
	s_cmpk_lt_u32 s2, 0x216
	s_cbranch_scc0 .LBB0_23
	v_and_b32_e32 v1, 0x7f, v0
	v_mov_b32_e32 v3, 0
	v_lshlrev_b32_e32 v2, 2, v1
	s_waitcnt lgkmcnt(0)
	v_lshl_add_u64 v[4:5], s[8:9], 0, v[2:3]
	v_add_co_u32_e32 v6, vcc, 0x3000, v4
	v_lshlrev_b32_e32 v1, 2, v0
	s_nop 0
	v_addc_co_u32_e32 v7, vcc, 0, v5, vcc
	v_add_co_u32_e32 v8, vcc, 0x2c000, v4
	v_or_b32_e32 v3, 0x2ce00, v1
	s_nop 0
	v_addc_co_u32_e32 v9, vcc, 0, v5, vcc
	global_load_dword v41, v[6:7], off offset:1536
	global_load_dword v39, v[6:7], off offset:2048
	global_load_dword v37, v[6:7], off offset:2560
	global_load_dword v36, v[8:9], off offset:1024
	global_load_dword v35, v[8:9], off offset:1536
	global_load_dword v34, v[8:9], off offset:2048
	global_load_dword v33, v[8:9], off offset:2560
	global_load_dword v32, v[8:9], off offset:3072
	v_add_co_u32_e32 v6, vcc, 0x2d000, v4
	s_load_dwordx2 s[4:5], s[0:1], 0x10
	s_nop 0
	v_addc_co_u32_e32 v7, vcc, 0, v5, vcc
	global_load_dword v42, v3, s[8:9]
	global_load_dword v44, v[6:7], off
	global_load_dword v43, v[6:7], off offset:512
	global_load_dword v40, v[6:7], off offset:1024
	global_load_dword v38, v[6:7], off offset:1536
	global_load_dword v26, v[6:7], off offset:2048
	global_load_dword v27, v[6:7], off offset:2560
	global_load_dword v28, v[6:7], off offset:3072
	v_add_co_u32_e32 v6, vcc, 0x2e000, v4
	v_or_b32_e32 v3, 0x2de00, v1
	s_nop 0
	v_addc_co_u32_e32 v7, vcc, 0, v5, vcc
	global_load_dword v24, v3, s[8:9]
	global_load_dword v29, v[6:7], off
	global_load_dword v30, v[6:7], off offset:512
	global_load_dword v31, v[6:7], off offset:1024
	global_load_dword v25, v[6:7], off offset:1536
	global_load_dword v18, v[6:7], off offset:2048
	global_load_dword v19, v[6:7], off offset:2560
	global_load_dword v20, v[6:7], off offset:3072
	v_add_co_u32_e32 v6, vcc, 0x2f000, v4
	v_or_b32_e32 v3, 0x2ee00, v1
	s_nop 0
	v_addc_co_u32_e32 v7, vcc, 0, v5, vcc
	global_load_dword v16, v3, s[8:9]
	global_load_dword v21, v[6:7], off
	global_load_dword v22, v[6:7], off offset:512
	global_load_dword v23, v[6:7], off offset:1024
	global_load_dword v17, v[6:7], off offset:1536
	global_load_dword v10, v[6:7], off offset:2048
	global_load_dword v11, v[6:7], off offset:2560
	global_load_dword v12, v[6:7], off offset:3072
	v_or_b32_e32 v3, 0x2fe00, v1
	v_add_co_u32_e32 v4, vcc, 0x30000, v4
	s_lshl_b32 s3, s2, 3
	s_nop 0
	v_addc_co_u32_e32 v5, vcc, 0, v5, vcc
	global_load_dword v7, v3, s[8:9]
	global_load_dword v13, v[4:5], off
	global_load_dword v14, v[4:5], off offset:512
	global_load_dword v15, v[4:5], off offset:1024
	global_load_dword v9, v[4:5], off offset:1536
	global_load_dword v8, v[4:5], off offset:2048
	global_load_dword v6, v[4:5], off offset:2560
	s_waitcnt lgkmcnt(0)
	global_load_dword v1, v2, s[4:5]
	s_load_dwordx2 s[4:5], s[0:1], 0x0
	s_addk_i32 s3, 0xff50
	v_or_b32_e32 v3, 0x100, v0
	v_mul_u32_u24_e32 v46, 0x691, v0
	v_mul_u32_u24_e32 v55, 0x691, v3
	v_lshrrev_b32_e32 v46, 16, v46
	v_lshrrev_b32_e32 v55, 16, v55
	v_mul_u32_u24_e32 v4, 39, v46
	v_mul_u32_u24_e32 v5, 39, v55
	v_sub_u32_e32 v45, v0, v4
	v_sub_u32_e32 v54, v3, v5
	v_cmp_gt_u32_e32 vcc, 21, v45
	v_add_u32_e32 v4, -3, v45
	v_add_u32_e32 v5, -21, v45
	s_mov_b64 s[12:13], vcc
	v_cndmask_b32_e32 v47, v5, v4, vcc
	v_cmp_gt_u32_e32 vcc, 3, v45
	v_mul_u32_u24_e32 v48, 43, v47
	v_lshrrev_b32_e32 v48, 8, v48
	s_mov_b64 s[14:15], vcc
	v_mul_u32_u24_e32 v4, 6, v48
	v_sub_u32_e32 v49, v47, v4
	v_cndmask_b32_e32 v48, v48, v45, vcc
	v_add_u32_e32 v50, s3, v46
	v_lshl_add_u32 v50, v50, 1, v50
	v_add_u32_e32 v50, v50, v48
	v_lshlrev_b32_e32 v50, 2, v50
	v_lshlrev_b32_e64 v51, v49, 1
	v_cvt_f32_u32_e32 v51, v51
	v_mul_f32_e32 v51, 0.15915494, v51
	v_mul_u32_u24_e32 v53, 0xa0, v46
	v_lshl_add_u32 v53, v45, 2, v53
	v_cmp_gt_u32_e32 vcc, 21, v54
	v_add_u32_e32 v4, -3, v54
	v_add_u32_e32 v5, -21, v54
	s_mov_b64 s[16:17], vcc
	v_cndmask_b32_e32 v56, v5, v4, vcc
	v_cmp_gt_u32_e32 vcc, 3, v54
	v_mul_u32_u24_e32 v57, 43, v56
	v_lshrrev_b32_e32 v57, 8, v57
	s_mov_b64 s[18:19], vcc
	v_mul_u32_u24_e32 v4, 6, v57
	v_sub_u32_e32 v58, v56, v4
	v_cndmask_b32_e32 v57, v57, v54, vcc
	v_add_u32_e32 v59, s3, v55
	v_lshl_add_u32 v59, v59, 1, v59
	v_add_u32_e32 v59, v59, v57
	v_lshlrev_b32_e32 v59, 2, v59
	v_lshlrev_b32_e64 v60, v58, 1
	v_cvt_f32_u32_e32 v60, v60
	v_mul_f32_e32 v60, 0.15915494, v60
	v_mul_u32_u24_e32 v62, 0xa0, v55
	v_lshl_add_u32 v62, v54, 2, v62
	s_waitcnt lgkmcnt(0)
	global_load_dword v52, v50, s[4:5]
	v_cmp_gt_u32_e32 vcc, 56, v0
	s_and_saveexec_b64 s[10:11], vcc
	s_cbranch_execz .Lenc_skip1
	global_load_dword v61, v59, s[4:5]
.Lenc_skip1:
	s_or_b64 exec, exec, s[10:11]
	s_waitcnt vmcnt(0)
	v_mul_f32_e32 v51, v51, v52
	v_sin_f32_e32 v4, v51
	v_cos_f32_e32 v5, v51
	s_nop 0
	v_cndmask_b32_e64 v4, v5, v4, s[12:13]
	v_cndmask_b32_e64 v4, v4, v52, s[14:15]
	ds_write_b32 v53, v4
	s_and_saveexec_b64 s[10:11], vcc
	s_cbranch_execz .Lenc_skip2
	s_waitcnt vmcnt(0)
	v_mul_f32_e32 v60, v60, v61
	v_sin_f32_e32 v4, v60
	v_cos_f32_e32 v5, v60
	s_nop 0
	v_cndmask_b32_e64 v4, v5, v4, s[16:17]
	v_cndmask_b32_e64 v4, v4, v61, s[18:19]
	ds_write_b32 v62, v4
